# P1 conv tiles 10032->9804 (3 fewer per converter WG), P7 tail 1360->1588
# speedup vs baseline: 1.0064x; 1.0013x over previous
.LBB0_86:
	s_cmp_lt_i32 s50, 2
	s_cselect_b64 s[6:7], -1, 0
	s_and_b64 s[0:1], s[6:7], s[2:3]
	s_andn2_b64 vcc, exec, s[0:1]
	v_writelane_b32 v254, s60, 4
	s_cbranch_vccnz .LBB0_260
	s_mov_b64 s[2:3], s[80:81]
	s_load_dwordx2 s[8:9], s[2:3], 0xa8
	s_cmpk_lg_i32 s56, 0x100
	s_cselect_b32 s0, s56, 0xb4
	s_cmp_ge_i32 s78, s0
	s_mov_b64 s[4:5], -1
	s_cbranch_scc0 .LBB0_145
	s_sub_i32 s1, s78, s0
	s_cmpk_gt_i32 s1, 0x264b
	s_cbranch_scc1 .LBB0_144
	s_sub_i32 s20, s56, s0
	s_abs_i32 s4, s20
	v_cvt_f32_u32_e32 v1, s4
	s_load_dwordx2 s[10:11], s[2:3], 0x78
	s_load_dwordx2 s[12:13], s[2:3], 0x88
	s_sub_i32 s2, s20, s1
	s_add_i32 s3, s2, 0x264b
	v_rcp_iflag_f32_e32 v1, v1
	s_sub_i32 s2, 0xffffd9b5, s2
	s_xor_b32 s14, s3, s20
	s_sub_i32 s5, 0, s4
	v_mul_f32_e32 v1, 0x4f7ffffe, v1
	v_cvt_u32_f32_e32 v1, v1
	s_max_i32 s2, s3, s2
	s_ashr_i32 s3, s14, 31
	v_readfirstlane_b32 s14, v1
	s_mul_i32 s5, s5, s14
	s_mul_hi_u32 s5, s14, s5
	s_add_i32 s14, s14, s5
	s_mul_hi_u32 s5, s2, s14
	s_mul_i32 s14, s5, s4
	s_sub_i32 s2, s2, s14
	s_add_i32 s14, s5, 1
	s_sub_i32 s15, s2, s4
	s_cmp_ge_u32 s2, s4
	s_cselect_b32 s5, s14, s5
	s_cselect_b32 s2, s15, s2
	s_add_i32 s14, s5, 1
	s_cmp_ge_u32 s2, s4
	s_cselect_b32 s2, s14, s5
	s_xor_b32 s2, s2, s3
	s_sub_i32 s29, s2, s3
	s_lshl_b32 s21, s29, 2
	s_add_i32 s22, s21, -1
	s_cmp_gt_i32 s29, 0
	s_cselect_b64 s[2:3], -1, 0
	s_and_b64 s[4:5], s[2:3], exec
	s_cselect_b32 s18, 0, s22
	s_ashr_i32 s4, s18, 2
	s_mul_i32 s17, s4, s20
	s_add_i32 s17, s17, s1
	s_cmpk_gt_i32 s17, 0x1fff
	s_mov_b32 s5, 0
	s_cbranch_scc0 .LBB0_91
	s_add_i32 s4, s17, 0xffffe000
	s_lshr_b32 s4, s4, 7
	s_lshl_b64 s[4:5], s[4:5], 24
	s_waitcnt lgkmcnt(0)
	s_add_u32 s14, s12, s4
	s_addc_u32 s15, s13, s5
	s_lshl_b32 s4, s17, 4
	s_and_b32 s26, s4, 0x780
	s_lshl_b32 s4, s17, 8
	s_and_b32 s16, s4, 0x700
	s_mov_b64 s[4:5], 0x800
	s_cbranch_execz .LBB0_92
	s_branch .LBB0_93

.LBB0_367:
	s_lshr_b32 s0, s56, 31
	s_add_i32 s0, s56, s0
	s_ashr_i32 s0, s0, 1
	v_readlane_b32 s78, v254, 5
	s_cmp_ge_i32 s78, s0
	v_readlane_b32 s79, v254, 8
	v_readlane_b32 s60, v254, 4
	s_cbranch_scc0 .LBB0_409
	s_sub_i32 s10, s78, s0
	s_cmpk_gt_u32 s10, 0x37f
	s_waitcnt vmcnt(0) lgkmcnt(0)
	s_barrier
	s_cbranch_scc1 .LBB0_409
	s_sub_i32 s0, s56, s0
	s_abs_i32 s2, s0
	v_cvt_f32_u32_e32 v2, s2
	s_sub_i32 s3, s0, s10
	s_add_i32 s4, s3, 0x37f
	s_sub_i32 s3, 0xfffffc81, s3
	v_rcp_iflag_f32_e32 v2, v2
	s_xor_b32 s6, s4, s0
	s_sub_i32 s5, 0, s2
	s_max_i32 s3, s4, s3
	v_mul_f32_e32 v2, 0x4f7ffffe, v2
	v_cvt_u32_f32_e32 v2, v2
	s_ashr_i32 s4, s6, 31
	s_add_i32 s1, s10, 0x264c
	v_readfirstlane_b32 s6, v2
	s_mul_i32 s5, s5, s6
	s_mul_hi_u32 s5, s6, s5
	s_add_i32 s6, s6, s5
	s_mul_hi_u32 s5, s3, s6
	s_mul_i32 s6, s5, s2
	s_sub_i32 s3, s3, s6
	s_add_i32 s7, s5, 1
	s_sub_i32 s6, s3, s2
	s_cmp_ge_u32 s3, s2
	s_cselect_b32 s5, s7, s5
	s_cselect_b32 s3, s6, s3
	s_add_i32 s6, s5, 1
	s_cmp_ge_u32 s3, s2
	s_cselect_b32 s2, s6, s5
	s_xor_b32 s2, s2, s4
	s_sub_i32 s18, s2, s4
	s_lshl_b32 s12, s18, 2
	s_add_i32 s13, s12, -1
	s_cmp_gt_i32 s18, 0
	s_cselect_b64 s[2:3], -1, 0
	s_and_b64 s[4:5], s[2:3], exec
	s_cselect_b32 s11, 0, s13
	s_ashr_i32 s4, s11, 2
	s_mul_i32 s9, s4, s0
	s_add_i32 s9, s9, s1
	s_cmpk_gt_i32 s9, 0x1fff
	s_mov_b32 s5, 0
	s_cbranch_scc0 .LBB0_371
	s_add_i32 s4, s9, 0xffffe000
	s_lshr_b32 s4, s4, 7
	s_lshl_b64 s[4:5], s[4:5], 24
	v_readlane_b32 s34, v254, 13
	v_readlane_b32 s35, v254, 14
	s_add_u32 s6, s34, s4
	s_addc_u32 s7, s35, s5
	s_lshl_b32 s4, s9, 4
	s_and_b32 s19, s4, 0x780
	s_lshl_b32 s4, s9, 8
	v_readlane_b32 s30, v254, 11
	s_and_b32 s8, s4, 0x700
	v_readlane_b32 s31, v254, 12
	s_mov_b64 s[4:5], 0x800
	s_cbranch_execz .LBB0_372
	s_branch .LBB0_373

.LBB0_387:
	s_max_i32 s9, s12, 1
	s_add_u32 s18, s66, 0x5ee00000
	s_addc_u32 s19, s67, 0
	s_ashr_i32 s7, s6, 31
	s_lshl_b64 s[6:7], s[6:7], 2
	s_add_u32 s4, s4, s6
	v_add_u32_e32 v3, s8, v14
	v_mov_b32_e32 v11, 0
	s_addc_u32 s5, s5, s7
	v_mad_i64_i32 v[12:13], s[6:7], s2, v3, 0
	v_lshl_add_u64 v[12:13], v[12:13], 2, s[4:5]
	v_mov_b32_e32 v3, v11
	v_lshl_add_u64 v[12:13], v[12:13], 0, v[2:3]
	s_mov_b64 s[6:7], 0x300
	s_add_i32 s27, 0, 0x18000
	v_lshl_add_u64 v[12:13], v[12:13], 0, s[6:7]
	s_add_i32 m0, s27, s14
	v_add_u32_e32 v3, s8, v15
	global_load_lds_dwordx4 v[12:13], off nt
	v_mad_i64_i32 v[12:13], s[28:29], s2, v3, 0
	v_lshl_add_u64 v[12:13], v[12:13], 2, s[4:5]
	v_mov_b32_e32 v5, v11
	v_lshl_add_u64 v[12:13], v[12:13], 0, v[4:5]
	v_lshl_add_u64 v[12:13], v[12:13], 0, s[6:7]
	s_add_i32 m0, s27, s15
	v_add_u32_e32 v3, s8, v16
	global_load_lds_dwordx4 v[12:13], off nt
	v_mad_i64_i32 v[12:13], s[28:29], s2, v3, 0
	v_lshl_add_u64 v[12:13], v[12:13], 2, s[4:5]
	v_mov_b32_e32 v7, v11
	v_lshl_add_u64 v[12:13], v[12:13], 0, v[6:7]
	v_lshl_add_u64 v[12:13], v[12:13], 0, s[6:7]
	s_add_i32 m0, s27, s16
	v_add_u32_e32 v3, s8, v1
	global_load_lds_dwordx4 v[12:13], off nt
	v_mad_i64_i32 v[12:13], s[2:3], s2, v3, 0
	v_lshl_add_u64 v[12:13], v[12:13], 2, s[4:5]
	v_mov_b32_e32 v9, v11
	v_lshl_add_u64 v[12:13], v[12:13], 0, v[8:9]
	v_lshl_add_u64 v[12:13], v[12:13], 0, s[6:7]
	s_add_i32 m0, s27, s17
	v_lshrrev_b32_e32 v19, 3, v162
	global_load_lds_dwordx4 v[12:13], off nt
	v_readlane_b32 s2, v254, 15
	v_and_b32_e32 v3, 7, v0
	v_lshrrev_b32_e32 v9, 1, v162
	v_or_b32_e32 v17, s2, v19
	v_lshrrev_b32_e32 v7, 2, v17
	v_bitop3_b32 v7, v7, v0, 7 bitop3:0x78
	v_lshl_add_u32 v5, v3, 12, 0
	v_lshlrev_b32_e32 v7, 4, v7
	v_and_b32_e32 v9, 12, v9
	v_add3_u32 v18, v5, v7, v9
	ds_read2st64_b32 v[12:13], v18 offset1:1
	ds_read2st64_b32 v[20:21], v18 offset0:2 offset1:3
	ds_read2st64_b32 v[22:23], v18 offset0:4 offset1:5
	ds_read2st64_b32 v[24:25], v18 offset0:6 offset1:7
	v_lshlrev_b32_e32 v10, 4, v3
	s_lshl_b32 s2, s10, 15
	s_waitcnt lgkmcnt(0)
	v_mul_f32_e32 v7, 0x42000000, v20
	v_mul_f32_e32 v3, 0x42000000, v12
	v_mul_f32_e32 v5, 0x42000000, v13
	ds_read2st64_b32 v[12:13], v18 offset0:8 offset1:9
	v_mul_f32_e32 v9, 0x42000000, v21
	v_mul_f32_e32 v26, 0x42000000, v22
	v_mul_f32_e32 v27, 0x42000000, v23
	v_mul_f32_e32 v28, 0x42000000, v24
	v_mul_f32_e32 v29, 0x42000000, v25
	ds_read2st64_b32 v[20:21], v18 offset0:10 offset1:11
	ds_read2st64_b32 v[22:23], v18 offset0:12 offset1:13
	ds_read2st64_b32 v[24:25], v18 offset0:14 offset1:15
	s_add_i32 s2, s2, 0x3260000
	s_and_b32 s2, s2, 0x7c00000
	s_waitcnt lgkmcnt(0)
	v_mul_f32_e32 v30, 0x42000000, v12
	v_mul_f32_e32 v13, 0x42000000, v13
	v_mul_f32_e32 v31, 0x42000000, v20
	v_mul_f32_e32 v32, 0x42000000, v21
	v_mul_f32_e32 v33, 0x42000000, v22
	v_mul_f32_e32 v34, 0x42000000, v23
	v_mov_b32_e32 v20, v11
	v_mov_b32_e32 v21, v11
	v_mov_b32_e32 v22, v11
	v_mov_b32_e32 v23, v11
	s_add_u32 s4, s18, s2
	v_cvt_pk_fp8_f32 v20, v3, v5
	v_cvt_pk_fp8_f32 v21, v26, v27
	v_cvt_pk_fp8_f32 v22, v30, v13
	v_cvt_pk_fp8_f32 v23, v33, v34
	s_addc_u32 s5, s19, 0
	s_lshl_b32 s6, s1, 8
	s_and_b32 s6, s6, 0x700
	v_mul_f32_e32 v3, 0x42000000, v24
	v_mul_f32_e32 v5, 0x42000000, v25
	v_add_u32_e32 v12, s6, v17
	v_mov_b32_e32 v13, v11
	s_lshl_b32 s2, s1, 4
	v_cvt_pk_fp8_f32 v20, v7, v9 op_sel:[0,0,1]
	v_cvt_pk_fp8_f32 v21, v28, v29 op_sel:[0,0,1]
	v_cvt_pk_fp8_f32 v22, v31, v32 op_sel:[0,0,1]
	v_cvt_pk_fp8_f32 v23, v3, v5 op_sel:[0,0,1]
	v_lshlrev_b64 v[24:25], 11, v[12:13]
	s_mov_b32 s3, 0
	s_and_b32 s2, s2, 0x780
	v_lshl_add_u64 v[24:25], s[4:5], 0, v[24:25]
	v_lshl_add_u64 v[24:25], v[24:25], 0, s[2:3]
	v_lshl_add_u64 v[24:25], v[24:25], 0, v[10:11]
	s_cmp_eq_u32 s9, 1
	global_store_dwordx4 v[24:25], v[20:23], off nt
	s_cbranch_scc1 .LBB0_408
	s_min_i32 s27, s13, 4
	s_ashr_i32 s6, s27, 2
	s_waitcnt vmcnt(9)
	s_barrier
	s_mul_i32 s29, s6, s0
	s_add_i32 s29, s29, s1
	s_cmpk_lt_i32 s29, 0x2000
	s_cbranch_scc1 .LBB0_390
	s_add_i32 s6, s29, 0xffffe000
	s_lshr_b32 s6, s6, 7
	s_mov_b32 s7, 0
	s_lshl_b64 s[6:7], s[6:7], 24
	s_add_u32 s8, s34, s6
	s_addc_u32 s9, s35, s7
	s_lshl_b32 s6, s29, 4
	s_and_b32 s28, s6, 0x780
	s_lshl_b32 s6, s29, 8
	s_and_b32 s10, s6, 0x700
	s_mov_b64 s[6:7], 0
	s_branch .LBB0_391

.LBB0_734:
	s_add_u32 s10, s48, 0xc000
	v_lshrrev_b32_e32 v8, 6, v0
	v_and_b32_e32 v2, 0xfc, v1
	s_addc_u32 s11, s49, 0
	v_mul_u32_u24_e32 v1, 0x410, v8
	v_lshlrev_b32_e32 v4, 2, v2
	s_mov_b32 s4, 0x10400
	v_lshrrev_b32_e32 v39, 1, v0
	v_and_b32_e32 v5, 1, v0
	s_add_u32 s22, s16, 0x5ee00000
	v_add3_u32 v1, 0, v1, v4
	v_lshlrev_b32_e32 v4, 6, v5
	v_mad_u32_u24 v5, v5, s4, 0
	v_lshlrev_b32_e32 v7, 2, v39
	v_lshrrev_b32_e32 v6, 2, v0
	s_addc_u32 s23, s17, 0
	v_mov_b32_e32 v3, 0
	v_add3_u32 v40, v5, v4, v7
	v_lshlrev_b32_e32 v7, 7, v39
	s_movk_i32 s4, 0xff
	s_add_i32 s24, 0, 0x27fd0
	s_mov_b32 s5, 0
	v_cmp_eq_u32_e64 s[2:3], 0, v0
	v_or_b32_e32 v9, 8, v8
	v_add_u32_e32 v10, 0x2080, v1
	v_or_b32_e32 v11, 16, v8
	v_add_u32_e32 v12, 0x4100, v1
	v_or_b32_e32 v13, 24, v8
	v_add_u32_e32 v14, 0x6180, v1
	v_or_b32_e32 v15, 32, v8
	v_add_u32_e32 v16, 0x8200, v1
	v_or_b32_e32 v17, 40, v8
	v_add_u32_e32 v18, 0xa280, v1
	v_or_b32_e32 v19, 48, v8
	v_add_u32_e32 v20, 0xc300, v1
	v_or_b32_e32 v21, 56, v8
	v_add_u32_e32 v22, 0xe380, v1
	v_or_b32_e32 v23, 64, v8
	v_add_u32_e32 v24, 0x10400, v1
	v_or_b32_e32 v25, 0x48, v8
	v_add_u32_e32 v26, 0x12480, v1
	v_or_b32_e32 v27, 0x50, v8
	v_add_u32_e32 v28, 0x14500, v1
	v_or_b32_e32 v29, 0x58, v8
	v_add_u32_e32 v30, 0x16580, v1
	v_or_b32_e32 v31, 0x60, v8
	v_add_u32_e32 v32, 0x18600, v1
	v_or_b32_e32 v33, 0x68, v8
	v_add_u32_e32 v34, 0x1a680, v1
	v_or_b32_e32 v35, 0x70, v8
	v_add_u32_e32 v36, 0x1c700, v1
	v_or_b32_e32 v37, 0x78, v8
	v_add_u32_e32 v38, 0x1e7c0, v1
	v_mov_b32_e32 v5, v3
	v_bitop3_b32 v41, v7, s4, v6 bitop3:0xc8
	v_mov_b32_e32 v42, s24
	s_movk_i32 s25, 0x633
	v_lshlrev_b32_e32 v2, 2, v2
	s_branch .LBB0_737

.LBB0_741:
	s_or_b64 exec, exec, s[16:17]
	s_waitcnt lgkmcnt(0)
	s_barrier
	ds_read_b32 v6, v42
	s_mov_b64 s[16:17], -1
	s_waitcnt lgkmcnt(0)
	v_cmp_lt_i32_e32 vcc, s25, v6
	v_readfirstlane_b32 s4, v6
	s_cbranch_vccnz .LBB0_736
	s_add_i32 s18, s4, 0x29cc
	s_cmpk_gt_i32 s4, 0xf633
	s_cbranch_scc0 .LBB0_744
	s_addk_i32 s4, 0x9cc
	s_lshr_b32 s4, s4, 7
	s_lshl_b64 s[16:17], s[4:5], 22
	s_lshl_b64 s[20:21], s[4:5], 24
	s_add_u32 s19, s14, s20
	s_addc_u32 s21, s15, s21
	s_add_u32 s16, s22, s16
	s_addc_u32 s17, s23, s17
	s_lshl_b32 s20, s18, 8
	s_lshl_b32 s4, s18, 4
	s_and_b32 s27, s20, 0x700
	s_and_b32 s26, s4, 0x7f0
	s_and_b32 s4, s4, 0x780
	s_lshl_b32 s20, s27, 2
	s_add_u32 s20, s19, s20
	s_addc_u32 s21, s21, 0
	v_or_b32_e32 v43, s4, v8
	v_lshl_add_u64 v[6:7], s[20:21], 0, v[2:3]
	v_lshlrev_b32_e32 v44, 13, v43
	v_mov_b32_e32 v45, v3
	v_or_b32_e32 v43, s4, v9
	v_lshl_add_u64 v[52:53], v[6:7], 0, v[44:45]
	v_lshlrev_b32_e32 v44, 13, v43
	v_or_b32_e32 v43, s4, v11
	v_lshl_add_u64 v[54:55], v[6:7], 0, v[44:45]
	global_load_dwordx4 v[44:47], v[52:53], off
	global_load_dwordx4 v[48:51], v[54:55], off
	v_lshlrev_b32_e32 v52, 13, v43
	v_mov_b32_e32 v53, v3
	v_or_b32_e32 v43, s4, v13
	v_lshl_add_u64 v[60:61], v[6:7], 0, v[52:53]
	v_lshlrev_b32_e32 v52, 13, v43
	v_or_b32_e32 v43, s4, v15
	v_lshl_add_u64 v[62:63], v[6:7], 0, v[52:53]
	global_load_dwordx4 v[52:55], v[60:61], off
	global_load_dwordx4 v[56:59], v[62:63], off
	v_lshlrev_b32_e32 v60, 13, v43
	v_mov_b32_e32 v61, v3
	v_or_b32_e32 v43, s4, v17
	v_lshl_add_u64 v[68:69], v[6:7], 0, v[60:61]
	v_lshlrev_b32_e32 v60, 13, v43
	v_or_b32_e32 v43, s4, v19
	v_lshl_add_u64 v[70:71], v[6:7], 0, v[60:61]
	global_load_dwordx4 v[60:63], v[68:69], off
	global_load_dwordx4 v[64:67], v[70:71], off
	v_lshlrev_b32_e32 v68, 13, v43
	v_mov_b32_e32 v69, v3
	v_or_b32_e32 v43, s4, v21
	v_lshl_add_u64 v[76:77], v[6:7], 0, v[68:69]
	v_lshlrev_b32_e32 v68, 13, v43
	v_or_b32_e32 v43, s4, v23
	v_lshl_add_u64 v[78:79], v[6:7], 0, v[68:69]
	global_load_dwordx4 v[68:71], v[76:77], off
	global_load_dwordx4 v[72:75], v[78:79], off
	v_lshlrev_b32_e32 v76, 13, v43
	v_mov_b32_e32 v77, v3
	v_or_b32_e32 v43, s4, v25
	v_lshl_add_u64 v[84:85], v[6:7], 0, v[76:77]
	v_lshlrev_b32_e32 v76, 13, v43
	v_or_b32_e32 v43, s4, v27
	v_lshl_add_u64 v[86:87], v[6:7], 0, v[76:77]
	global_load_dwordx4 v[76:79], v[84:85], off
	global_load_dwordx4 v[80:83], v[86:87], off
	v_lshlrev_b32_e32 v84, 13, v43
	v_mov_b32_e32 v85, v3
	v_or_b32_e32 v43, s4, v29
	v_lshl_add_u64 v[92:93], v[6:7], 0, v[84:85]
	v_lshlrev_b32_e32 v84, 13, v43
	v_or_b32_e32 v43, s4, v31
	v_lshl_add_u64 v[94:95], v[6:7], 0, v[84:85]
	global_load_dwordx4 v[84:87], v[92:93], off
	global_load_dwordx4 v[88:91], v[94:95], off
	v_lshlrev_b32_e32 v92, 13, v43
	v_mov_b32_e32 v93, v3
	v_or_b32_e32 v43, s4, v33
	v_lshl_add_u64 v[100:101], v[6:7], 0, v[92:93]
	v_lshlrev_b32_e32 v92, 13, v43
	v_or_b32_e32 v43, s26, v35
	v_lshl_add_u64 v[102:103], v[6:7], 0, v[92:93]
	global_load_dwordx4 v[92:95], v[100:101], off
	global_load_dwordx4 v[96:99], v[102:103], off
	v_lshlrev_b32_e32 v100, 13, v43
	v_mov_b32_e32 v101, v3
	v_or_b32_e32 v43, s4, v37
	v_lshl_add_u64 v[108:109], v[6:7], 0, v[100:101]
	v_lshlrev_b32_e32 v100, 13, v43
	v_lshl_add_u64 v[6:7], v[6:7], 0, v[100:101]
	global_load_dwordx4 v[100:103], v[108:109], off
	global_load_dwordx4 v[104:107], v[6:7], off
	v_or_b32_e32 v6, s27, v39
	v_lshlrev_b32_e32 v6, 11, v6
	v_mov_b32_e32 v7, v3
	v_lshl_add_u64 v[6:7], s[16:17], 0, v[6:7]
	v_lshl_add_u64 v[6:7], v[6:7], 0, s[4:5]
	v_lshl_add_u64 v[6:7], v[6:7], 0, v[4:5]
	s_mov_b64 s[16:17], 0
	s_waitcnt vmcnt(15)
	ds_write_b128 v1, v[44:47]
	s_waitcnt vmcnt(14)
	ds_write_b128 v10, v[48:51]
	s_waitcnt vmcnt(13)
	ds_write_b128 v12, v[52:55]
	s_waitcnt vmcnt(12)
	ds_write_b128 v14, v[56:59]
	s_waitcnt vmcnt(11)
	ds_write_b128 v16, v[60:63]
	s_waitcnt vmcnt(10)
	ds_write_b128 v18, v[64:67]
	s_waitcnt vmcnt(9)
	ds_write_b128 v20, v[68:71]
	s_waitcnt vmcnt(8)
	ds_write_b128 v22, v[72:75]
	s_waitcnt vmcnt(7)
	ds_write_b128 v24, v[76:79] offset:64
	s_waitcnt vmcnt(6)
	ds_write_b128 v26, v[80:83] offset:64
	s_waitcnt vmcnt(5)
	ds_write_b128 v28, v[84:87] offset:64
	s_waitcnt vmcnt(4)
	ds_write_b128 v30, v[88:91] offset:64
	s_waitcnt vmcnt(3)
	ds_write_b128 v32, v[92:95] offset:64
	s_waitcnt vmcnt(2)
	ds_write_b128 v34, v[96:99] offset:64
	s_waitcnt vmcnt(1)
	ds_write_b128 v36, v[100:103] offset:64
	s_waitcnt vmcnt(0)
	ds_write_b128 v38, v[104:107]
	s_waitcnt lgkmcnt(0)
	s_barrier
	ds_read_b32 v43, v40
	ds_read_b32 v44, v40 offset:1040
	ds_read_b32 v45, v40 offset:2080
	ds_read_b32 v46, v40 offset:3120
	ds_read_b32 v47, v40 offset:4160
	ds_read_b32 v48, v40 offset:5200
	ds_read_b32 v49, v40 offset:6240
	ds_read_b32 v50, v40 offset:7280
	s_waitcnt lgkmcnt(6)
	v_mul_f32_e32 v51, 0x42000000, v44
	s_waitcnt lgkmcnt(5)
	v_mul_f32_e32 v52, 0x42000000, v45
	s_waitcnt lgkmcnt(4)
	v_mul_f32_e32 v53, 0x42000000, v46
	s_waitcnt lgkmcnt(3)
	v_mul_f32_e32 v46, 0x42000000, v47
	s_waitcnt lgkmcnt(2)
	v_mul_f32_e32 v47, 0x42000000, v48
	s_waitcnt lgkmcnt(1)
	v_mul_f32_e32 v48, 0x42000000, v49
	s_waitcnt lgkmcnt(0)
	v_mul_f32_e32 v49, 0x42000000, v50
	ds_read_b32 v44, v40 offset:8320
	ds_read_b32 v45, v40 offset:9360
	ds_read_b32 v50, v40 offset:10400
	ds_read_b32 v54, v40 offset:11440
	ds_read_b32 v55, v40 offset:12480
	ds_read_b32 v56, v40 offset:13520
	ds_read_b32 v57, v40 offset:14560
	ds_read_b32 v58, v40 offset:15600
	s_waitcnt lgkmcnt(6)
	v_mul_f32_e32 v60, 0x42000000, v45
	v_mov_b32_e32 v45, v3
	v_mul_f32_e32 v43, 0x42000000, v43
	v_mul_f32_e32 v59, 0x42000000, v44
	v_mov_b32_e32 v44, v3
	v_cvt_pk_fp8_f32 v45, v46, v47
	v_mov_b32_e32 v46, v3
	v_cvt_pk_fp8_f32 v44, v43, v51
	v_cvt_pk_fp8_f32 v46, v59, v60
	s_waitcnt lgkmcnt(5)
	v_mul_f32_e32 v50, 0x42000000, v50
	s_waitcnt lgkmcnt(4)
	v_mul_f32_e32 v54, 0x42000000, v54
	s_waitcnt lgkmcnt(3)
	v_mul_f32_e32 v55, 0x42000000, v55
	s_waitcnt lgkmcnt(2)
	v_mul_f32_e32 v56, 0x42000000, v56
	v_mov_b32_e32 v47, v3
	v_cvt_pk_fp8_f32 v44, v52, v53 op_sel:[0,0,1]
	v_cvt_pk_fp8_f32 v45, v48, v49 op_sel:[0,0,1]
	v_cvt_pk_fp8_f32 v46, v50, v54 op_sel:[0,0,1]
	ds_read_b32 v43, v40 offset:16640
	ds_read_b32 v48, v40 offset:17680
	ds_read_b32 v49, v40 offset:18720
	ds_read_b32 v50, v40 offset:19760
	ds_read_b32 v51, v40 offset:20800
	ds_read_b32 v52, v40 offset:21840
	ds_read_b32 v53, v40 offset:22880
	ds_read_b32 v54, v40 offset:23920
	v_cvt_pk_fp8_f32 v47, v55, v56
	s_waitcnt lgkmcnt(9)
	v_mul_f32_e32 v57, 0x42000000, v57
	s_waitcnt lgkmcnt(8)
	v_mul_f32_e32 v58, 0x42000000, v58
	s_waitcnt lgkmcnt(6)
	v_mul_f32_e32 v55, 0x42000000, v48
	v_cvt_pk_fp8_f32 v47, v57, v58 op_sel:[0,0,1]
	s_waitcnt lgkmcnt(5)
	v_mul_f32_e32 v56, 0x42000000, v49
	s_waitcnt lgkmcnt(4)
	v_mul_f32_e32 v57, 0x42000000, v50
	s_waitcnt lgkmcnt(3)
	v_mul_f32_e32 v50, 0x42000000, v51
	s_waitcnt lgkmcnt(2)
	v_mul_f32_e32 v51, 0x42000000, v52
	s_waitcnt lgkmcnt(1)
	v_mul_f32_e32 v52, 0x42000000, v53
	s_waitcnt lgkmcnt(0)
	v_mul_f32_e32 v53, 0x42000000, v54
	ds_read_b32 v48, v40 offset:24960
	ds_read_b32 v49, v40 offset:26000
	ds_read_b32 v54, v40 offset:27040
	ds_read_b32 v58, v40 offset:28080
	ds_read_b32 v59, v40 offset:29120
	ds_read_b32 v60, v40 offset:30160
	ds_read_b32 v61, v40 offset:31200
	ds_read_b32 v62, v40 offset:32240
	s_waitcnt lgkmcnt(6)
	v_mul_f32_e32 v64, 0x42000000, v49
	v_mov_b32_e32 v49, v3
	v_mul_f32_e32 v43, 0x42000000, v43
	v_mul_f32_e32 v63, 0x42000000, v48
	v_mov_b32_e32 v48, v3
	v_cvt_pk_fp8_f32 v49, v50, v51
	v_mov_b32_e32 v50, v3
	v_cvt_pk_fp8_f32 v48, v43, v55
	v_cvt_pk_fp8_f32 v50, v63, v64
	s_waitcnt lgkmcnt(5)
	v_mul_f32_e32 v54, 0x42000000, v54
	s_waitcnt lgkmcnt(4)
	v_mul_f32_e32 v58, 0x42000000, v58
	s_waitcnt lgkmcnt(3)
	v_mul_f32_e32 v59, 0x42000000, v59
	s_waitcnt lgkmcnt(2)
	v_mul_f32_e32 v60, 0x42000000, v60
	v_mov_b32_e32 v51, v3
	v_cvt_pk_fp8_f32 v48, v56, v57 op_sel:[0,0,1]
	v_cvt_pk_fp8_f32 v49, v52, v53 op_sel:[0,0,1]
	v_cvt_pk_fp8_f32 v50, v54, v58 op_sel:[0,0,1]
	ds_read_b32 v43, v40 offset:33280
	ds_read_b32 v52, v40 offset:34320
	ds_read_b32 v53, v40 offset:35360
	ds_read_b32 v54, v40 offset:36400
	ds_read_b32 v55, v40 offset:37440
	ds_read_b32 v56, v40 offset:38480
	ds_read_b32 v57, v40 offset:39520
	ds_read_b32 v58, v40 offset:40560
	v_cvt_pk_fp8_f32 v51, v59, v60
	s_waitcnt lgkmcnt(9)
	v_mul_f32_e32 v61, 0x42000000, v61
	s_waitcnt lgkmcnt(8)
	v_mul_f32_e32 v62, 0x42000000, v62
	s_waitcnt lgkmcnt(6)
	v_mul_f32_e32 v59, 0x42000000, v52
	v_cvt_pk_fp8_f32 v51, v61, v62 op_sel:[0,0,1]
	s_waitcnt lgkmcnt(5)
	v_mul_f32_e32 v60, 0x42000000, v53
	s_waitcnt lgkmcnt(4)
	v_mul_f32_e32 v61, 0x42000000, v54
	s_waitcnt lgkmcnt(3)
	v_mul_f32_e32 v54, 0x42000000, v55
	s_waitcnt lgkmcnt(2)
	v_mul_f32_e32 v55, 0x42000000, v56
	s_waitcnt lgkmcnt(1)
	v_mul_f32_e32 v56, 0x42000000, v57
	s_waitcnt lgkmcnt(0)
	v_mul_f32_e32 v57, 0x42000000, v58
	ds_read_b32 v52, v40 offset:41600
	ds_read_b32 v53, v40 offset:42640
	ds_read_b32 v58, v40 offset:43680
	ds_read_b32 v62, v40 offset:44720
	ds_read_b32 v63, v40 offset:45760
	ds_read_b32 v64, v40 offset:46800
	ds_read_b32 v65, v40 offset:47840
	ds_read_b32 v66, v40 offset:48880
	s_waitcnt lgkmcnt(6)
	v_mul_f32_e32 v68, 0x42000000, v53
	v_mov_b32_e32 v53, v3
	v_mul_f32_e32 v43, 0x42000000, v43
	v_mul_f32_e32 v67, 0x42000000, v52
	v_mov_b32_e32 v52, v3
	v_cvt_pk_fp8_f32 v53, v54, v55
	v_mov_b32_e32 v54, v3
	v_cvt_pk_fp8_f32 v52, v43, v59
	v_cvt_pk_fp8_f32 v54, v67, v68
	s_waitcnt lgkmcnt(5)
	v_mul_f32_e32 v58, 0x42000000, v58
	s_waitcnt lgkmcnt(4)
	v_mul_f32_e32 v62, 0x42000000, v62
	s_waitcnt lgkmcnt(3)
	v_mul_f32_e32 v63, 0x42000000, v63
	s_waitcnt lgkmcnt(2)
	v_mul_f32_e32 v64, 0x42000000, v64
	v_mov_b32_e32 v55, v3
	v_cvt_pk_fp8_f32 v52, v60, v61 op_sel:[0,0,1]
	v_cvt_pk_fp8_f32 v53, v56, v57 op_sel:[0,0,1]
	v_cvt_pk_fp8_f32 v54, v58, v62 op_sel:[0,0,1]
	ds_read_b32 v43, v40 offset:49920
	ds_read_b32 v56, v40 offset:50960
	ds_read_b32 v57, v40 offset:52000
	ds_read_b32 v58, v40 offset:53040
	ds_read_b32 v59, v40 offset:54080
	ds_read_b32 v60, v40 offset:55120
	ds_read_b32 v61, v40 offset:56160
	ds_read_b32 v62, v40 offset:57200
	v_cvt_pk_fp8_f32 v55, v63, v64
	s_waitcnt lgkmcnt(9)
	v_mul_f32_e32 v65, 0x42000000, v65
	s_waitcnt lgkmcnt(8)
	v_mul_f32_e32 v66, 0x42000000, v66
	s_waitcnt lgkmcnt(6)
	v_mul_f32_e32 v63, 0x42000000, v56
	v_cvt_pk_fp8_f32 v55, v65, v66 op_sel:[0,0,1]
	s_waitcnt lgkmcnt(5)
	v_mul_f32_e32 v64, 0x42000000, v57
	s_waitcnt lgkmcnt(4)
	v_mul_f32_e32 v65, 0x42000000, v58
	s_waitcnt lgkmcnt(3)
	v_mul_f32_e32 v58, 0x42000000, v59
	s_waitcnt lgkmcnt(2)
	v_mul_f32_e32 v59, 0x42000000, v60
	s_waitcnt lgkmcnt(1)
	v_mul_f32_e32 v60, 0x42000000, v61
	s_waitcnt lgkmcnt(0)
	v_mul_f32_e32 v61, 0x42000000, v62
	ds_read_b32 v56, v40 offset:58240
	ds_read_b32 v57, v40 offset:59280
	ds_read_b32 v62, v40 offset:60320
	ds_read_b32 v66, v40 offset:61360
	ds_read_b32 v67, v40 offset:62400
	ds_read_b32 v68, v40 offset:63440
	ds_read_b32 v69, v40 offset:64480
	ds_read_b32 v70, v40 offset:65520
	s_waitcnt lgkmcnt(6)
	v_mul_f32_e32 v72, 0x42000000, v57
	v_mov_b32_e32 v57, v3
	v_mul_f32_e32 v43, 0x42000000, v43
	v_mul_f32_e32 v71, 0x42000000, v56
	s_waitcnt lgkmcnt(3)
	v_mul_f32_e32 v67, 0x42000000, v67
	s_waitcnt lgkmcnt(2)
	v_mul_f32_e32 v68, 0x42000000, v68
	v_mov_b32_e32 v56, v3
	v_cvt_pk_fp8_f32 v57, v58, v59
	v_mov_b32_e32 v58, v3
	v_mov_b32_e32 v59, v3
	v_cvt_pk_fp8_f32 v56, v43, v63
	v_cvt_pk_fp8_f32 v58, v71, v72
	v_cvt_pk_fp8_f32 v59, v67, v68
	v_mul_f32_e32 v62, 0x42000000, v62
	v_mul_f32_e32 v66, 0x42000000, v66
	s_waitcnt lgkmcnt(1)
	v_mul_f32_e32 v69, 0x42000000, v69
	s_waitcnt lgkmcnt(0)
	v_mul_f32_e32 v70, 0x42000000, v70
	v_cvt_pk_fp8_f32 v56, v64, v65 op_sel:[0,0,1]
	v_cvt_pk_fp8_f32 v57, v60, v61 op_sel:[0,0,1]
	v_cvt_pk_fp8_f32 v58, v62, v66 op_sel:[0,0,1]
	v_cvt_pk_fp8_f32 v59, v69, v70 op_sel:[0,0,1]
	global_store_dwordx4 v[6:7], v[44:47], off
	global_store_dwordx4 v[6:7], v[48:51], off offset:16
	global_store_dwordx4 v[6:7], v[52:55], off offset:32
	global_store_dwordx4 v[6:7], v[56:59], off offset:48
	s_waitcnt lgkmcnt(0)
	s_barrier
